# speedup vs baseline: 1.0255x; 1.0049x over previous
_Z8k2_fusedPKDF16_PKDv8_DF16_PKfS5_S5_PfPiS6_:
	v_readfirstlane_b32 s38, v0
	s_load_dwordx8 s[4:11], s[0:1], 0x0
	s_load_dwordx4 s[32:35], s[0:1], 0x20
	s_load_dwordx2 s[36:37], s[0:1], 0x38
	s_lshl_b32 s3, s2, 2
	s_ashr_i32 s16, s2, 4
	s_and_b32 s12, s3, 48
	s_lshl_b32 s2, s2, 4
	s_and_b32 s13, s2, 48
	v_min_u32_e32 v48, 0x18f, v0
	v_mul_u32_u24_e32 v49, 0x334, v48
	v_lshrrev_b32_e32 v49, 16, v49
	v_mul_u32_u24_e32 v50, 0x50, v49
	v_sub_u32_e32 v50, v48, v50
	v_lshrrev_b32_e32 v51, 2, v50
	v_and_b32_e32 v46, 3, v50
	v_lshlrev_b32_e32 v46, 4, v46
	s_add_i32 s3, s13, -2
	v_add_u32_e32 v52, s3, v51
	v_cmp_gt_u32_e64 s[20:21], 64, v52
	v_med3_i32 v52, v52, 0, 63
	s_lshl_b32 s14, s16, 18
	v_lshl_or_b32 v52, v52, 6, v46
	v_or_b32_e32 v52, s14, v52
	s_add_i32 s2, s12, -2
	v_add_u32_e32 v53, s2, v49
	v_add_u32_e32 v54, 5, v53
	v_add_u32_e32 v55, 10, v53
	v_add_u32_e32 v56, 15, v53
	v_cmp_gt_u32_e64 s[40:41], 64, v53
	v_cmp_gt_u32_e64 s[42:43], 64, v54
	v_cmp_gt_u32_e64 s[44:45], 64, v55
	v_cmp_gt_u32_e64 s[46:47], 64, v56
	v_med3_i32 v53, v53, 0, 63
	v_med3_i32 v54, v54, 0, 63
	v_med3_i32 v55, v55, 0, 63
	v_med3_i32 v56, v56, 0, 63
	v_lshl_or_b32 v53, v53, 12, v52
	v_lshl_or_b32 v54, v54, 12, v52
	v_lshl_or_b32 v55, v55, 12, v52
	v_lshl_or_b32 v56, v56, 12, v52
	s_and_b64 s[40:41], s[40:41], s[20:21]
	s_and_b64 s[42:43], s[42:43], s[20:21]
	s_and_b64 s[44:45], s[44:45], s[20:21]
	s_and_b64 s[46:47], s[46:47], s[20:21]
	v_lshlrev_b32_e32 v85, 4, v0
	v_or_b32_e32 v57, 0x200, v0
	v_lshlrev_b32_e32 v87, 4, v57
	v_or_b32_e32 v58, 0x400, v0
	v_min_u32_e32 v57, 0x47f, v58
	v_lshlrev_b32_e32 v90, 4, v57
	v_lshrrev_b32_e32 v164, 1, v0
	v_and_b32_e32 v162, 16, v164
	v_and_b32_e32 v1, 63, v0
	v_and_b32_e32 v165, 31, v0
	v_lshrrev_b32_e32 v163, 6, v0
	v_mad_u32_u24 v47, v49, 20, v51
	s_movk_i32 s39, 0x50
	v_mad_u32_u24 v47, v47, s39, v46
	s_waitcnt lgkmcnt(0)
	global_load_dwordx4 v[18:21], v53, s[4:5]
	global_load_dwordx4 v[22:25], v54, s[4:5]
	global_load_dwordx4 v[26:29], v55, s[4:5]
	global_load_dwordx4 v[30:33], v56, s[4:5]
	global_load_dwordx4 v[34:37], v85, s[6:7]
	global_load_dwordx4 v[38:41], v87, s[6:7]
	global_load_dwordx4 v[42:45], v90, s[6:7]
	global_load_dwordx4 v[2:5], v162, s[8:9]
	global_load_dwordx4 v[6:9], v162, s[8:9] offset:32
	global_load_dwordx4 v[10:13], v162, s[8:9] offset:64
	global_load_dwordx4 v[14:17], v162, s[8:9] offset:96
	s_movk_i32 s8, 0x50
	s_lshr_b32 s27, s12, 1
	s_lshr_b32 s26, s13, 1
	v_add_u32_e32 v48, s27, v163
	v_bfe_u32 v49, v0, 1, 3
	v_add_u32_e32 v49, s26, v49
	v_lshlrev_b32_e32 v48, 10, v48
	v_lshl_or_b32 v48, v49, 5, v48
	v_bfe_u32 v49, v0, 5, 1
	v_lshl_or_b32 v48, v49, 2, v48
	v_bfe_u32 v49, v0, 4, 1
	v_lshl_or_b32 v48, v49, 1, v48
	v_and_b32_e32 v49, 1, v0
	v_or_b32_e32 v48, v48, v49
	v_mul_u32_u24_e32 v210, 40, v48
	s_cmp_lt_u32 s38, 0xc0
	s_cbranch_scc0 .Lk2_late
	global_load_dwordx4 v[66:69], v210, s[10:11]
	global_load_dwordx4 v[50:53], v210, s[10:11] offset:16
	global_load_dwordx2 v[156:157], v210, s[10:11] offset:32
	global_load_dwordx4 v[70:73], v210, s[10:11] offset:320
	global_load_dwordx4 v[54:57], v210, s[10:11] offset:336
	global_load_dwordx2 v[154:155], v210, s[10:11] offset:352
	global_load_dwordx4 v[74:77], v210, s[10:11] offset:640
	global_load_dwordx4 v[58:61], v210, s[10:11] offset:656
	global_load_dwordx2 v[160:161], v210, s[10:11] offset:672
	global_load_dwordx4 v[78:81], v210, s[10:11] offset:960
	global_load_dwordx4 v[62:65], v210, s[10:11] offset:976
	global_load_dwordx2 v[158:159], v210, s[10:11] offset:992
	s_waitcnt vmcnt(22)
	v_cndmask_b32_e64 v18, 0, v18, s[40:41]
	v_cndmask_b32_e64 v19, 0, v19, s[40:41]
	v_cndmask_b32_e64 v20, 0, v20, s[40:41]
	v_cndmask_b32_e64 v21, 0, v21, s[40:41]
	ds_write_b128 v47, v[18:21]
	s_waitcnt vmcnt(21)
	v_cndmask_b32_e64 v22, 0, v22, s[42:43]
	v_cndmask_b32_e64 v23, 0, v23, s[42:43]
	v_cndmask_b32_e64 v24, 0, v24, s[42:43]
	v_cndmask_b32_e64 v25, 0, v25, s[42:43]
	ds_write_b128 v47, v[22:25] offset:8000
	s_waitcnt vmcnt(20)
	v_cndmask_b32_e64 v26, 0, v26, s[44:45]
	v_cndmask_b32_e64 v27, 0, v27, s[44:45]
	v_cndmask_b32_e64 v28, 0, v28, s[44:45]
	v_cndmask_b32_e64 v29, 0, v29, s[44:45]
	ds_write_b128 v47, v[26:29] offset:16000
	s_waitcnt vmcnt(19)
	v_cndmask_b32_e64 v30, 0, v30, s[46:47]
	v_cndmask_b32_e64 v31, 0, v31, s[46:47]
	v_cndmask_b32_e64 v32, 0, v32, s[46:47]
	v_cndmask_b32_e64 v33, 0, v33, s[46:47]
	ds_write_b128 v47, v[30:33] offset:24000
	s_waitcnt vmcnt(18)
	ds_write_b128 v85, v[34:37] offset:57920
	s_waitcnt vmcnt(17)
	ds_write_b128 v87, v[38:41] offset:57920
	s_waitcnt vmcnt(16)
	ds_write_b128 v90, v[42:45] offset:57920
	s_branch .Lk2_stg_done
.Lk2_late:
	s_waitcnt vmcnt(10)
	v_cndmask_b32_e64 v18, 0, v18, s[40:41]
	v_cndmask_b32_e64 v19, 0, v19, s[40:41]
	v_cndmask_b32_e64 v20, 0, v20, s[40:41]
	v_cndmask_b32_e64 v21, 0, v21, s[40:41]
	ds_write_b128 v47, v[18:21]
	s_waitcnt vmcnt(9)
	v_cndmask_b32_e64 v22, 0, v22, s[42:43]
	v_cndmask_b32_e64 v23, 0, v23, s[42:43]
	v_cndmask_b32_e64 v24, 0, v24, s[42:43]
	v_cndmask_b32_e64 v25, 0, v25, s[42:43]
	ds_write_b128 v47, v[22:25] offset:8000
	s_waitcnt vmcnt(8)
	v_cndmask_b32_e64 v26, 0, v26, s[44:45]
	v_cndmask_b32_e64 v27, 0, v27, s[44:45]
	v_cndmask_b32_e64 v28, 0, v28, s[44:45]
	v_cndmask_b32_e64 v29, 0, v29, s[44:45]
	ds_write_b128 v47, v[26:29] offset:16000
	s_waitcnt vmcnt(7)
	v_cndmask_b32_e64 v30, 0, v30, s[46:47]
	v_cndmask_b32_e64 v31, 0, v31, s[46:47]
	v_cndmask_b32_e64 v32, 0, v32, s[46:47]
	v_cndmask_b32_e64 v33, 0, v33, s[46:47]
	ds_write_b128 v47, v[30:33] offset:24000
	s_waitcnt vmcnt(6)
	ds_write_b128 v85, v[34:37] offset:57920
	s_waitcnt vmcnt(5)
	ds_write_b128 v87, v[38:41] offset:57920
	s_waitcnt vmcnt(4)
	ds_write_b128 v90, v[42:45] offset:57920
